# same as previous hosted-fp6 version but the hosted blocks use the spare VGPRs v253/v254 as temporaries
# baseline (speedup 1.0000x reference)
; template <int MODE>
; __device__ __forceinline__ void tr_matrix6(const float* W, int nb, int K, int N, unsigned char* WT, int drows, int rot, int gw, int NGW, int lane, float wscale) {
;     ...
;     for (; it < total; it += NGW) {
;         const int e = it / per, r = it - e * per, kb = r / nbn, nbk = r - kb * nbn, n0 = nbk * 32, k0 = kb * 256;
;         const float* src = W + (size_t)e * K * N + (size_t)(k0 + 32 * q) * N + n0 + 4 * c;
;         f32x4 v[32];
; #pragma unroll
;         for (int i = 0; i < 32; ++i) v[i] = *(const f32x4*)(src + (size_t)i * N);
.LBB0_1037:
	s_and_b32 s18, s89, 3
	s_cmp_eq_u32 s18, 2
	s_cbranch_scc0 .Lf6_noload_a
	s_cmp_lt_i32 s98, s99
	s_cbranch_scc0 .Lf6_noload_a
	s_mul_hi_u32 s18, s98, 0x2492493
	s_mul_i32 s19, s18, 0x70
	s_sub_u32 s19, s98, s19
	s_and_b32 s20, s18, 63
	s_lshr_b32 s18, s18, 6
	s_and_b32 s21, s18, 3
	s_add_u32 s21, s21, 4
	s_lshr_b32 s18, s18, 2
	s_lshl_b32 s21, s21, 11
	s_lshl_b32 s20, s20, 5
	s_add_u32 s21, s21, s20
	s_mul_i32 s21, s21, 0x7000
	s_lshl_b32 s19, s19, 8
	s_add_u32 s21, s21, s19
	s_lshl_b32 s20, s18, 1
	s_nop 3
	v_readlane_b32 s18, v252, s20
	s_add_u32 s20, s20, 1
	s_nop 3
	v_readlane_b32 s19, v252, s20
	s_nop 3
	s_add_u32 s18, s18, s21
	s_addc_u32 s19, s19, 0
	v_mbcnt_lo_u32_b32 v253, -1, 0
	v_mbcnt_hi_u32_b32 v253, -1, v253
	v_lshlrev_b32_e32 v253, 2, v253
	global_load_dword v158, v253, s[18:19]
	s_add_u32 s18, s18, 0x7000
	s_addc_u32 s19, s19, 0
	global_load_dword v159, v253, s[18:19]
	s_add_u32 s18, s18, 0x7000
	s_addc_u32 s19, s19, 0
	global_load_dword v160, v253, s[18:19]
	s_add_u32 s18, s18, 0x7000
	s_addc_u32 s19, s19, 0
	global_load_dword v161, v253, s[18:19]
	s_add_u32 s18, s18, 0x7000
	s_addc_u32 s19, s19, 0
	global_load_dword v162, v253, s[18:19]
	s_add_u32 s18, s18, 0x7000
	s_addc_u32 s19, s19, 0
	global_load_dword v163, v253, s[18:19]
	s_add_u32 s18, s18, 0x7000
	s_addc_u32 s19, s19, 0
	global_load_dword v164, v253, s[18:19]
	s_add_u32 s18, s18, 0x7000
	s_addc_u32 s19, s19, 0
	global_load_dword v165, v253, s[18:19]
	s_add_u32 s18, s18, 0x7000
	s_addc_u32 s19, s19, 0
	global_load_dword v166, v253, s[18:19]
	s_add_u32 s18, s18, 0x7000
	s_addc_u32 s19, s19, 0
	global_load_dword v167, v253, s[18:19]
	s_add_u32 s18, s18, 0x7000
	s_addc_u32 s19, s19, 0
	global_load_dword v168, v253, s[18:19]
	s_add_u32 s18, s18, 0x7000
	s_addc_u32 s19, s19, 0
	global_load_dword v169, v253, s[18:19]
	s_add_u32 s18, s18, 0x7000
	s_addc_u32 s19, s19, 0
	global_load_dword v170, v253, s[18:19]
	s_add_u32 s18, s18, 0x7000
	s_addc_u32 s19, s19, 0
	global_load_dword v171, v253, s[18:19]
	s_add_u32 s18, s18, 0x7000
	s_addc_u32 s19, s19, 0
	global_load_dword v172, v253, s[18:19]
	s_add_u32 s18, s18, 0x7000
	s_addc_u32 s19, s19, 0
	global_load_dword v173, v253, s[18:19]
	s_add_u32 s18, s18, 0x7000
	s_addc_u32 s19, s19, 0
	global_load_dword v174, v253, s[18:19]
	s_add_u32 s18, s18, 0x7000
	s_addc_u32 s19, s19, 0
	global_load_dword v175, v253, s[18:19]
	s_add_u32 s18, s18, 0x7000
	s_addc_u32 s19, s19, 0
	global_load_dword v176, v253, s[18:19]
	s_add_u32 s18, s18, 0x7000
	s_addc_u32 s19, s19, 0
	global_load_dword v177, v253, s[18:19]
	s_add_u32 s18, s18, 0x7000
	s_addc_u32 s19, s19, 0
	global_load_dword v178, v253, s[18:19]
	s_add_u32 s18, s18, 0x7000
	s_addc_u32 s19, s19, 0
	global_load_dword v179, v253, s[18:19]
	s_add_u32 s18, s18, 0x7000
	s_addc_u32 s19, s19, 0
	global_load_dword v180, v253, s[18:19]
	s_add_u32 s18, s18, 0x7000
	s_addc_u32 s19, s19, 0
	global_load_dword v181, v253, s[18:19]
	s_add_u32 s18, s18, 0x7000
	s_addc_u32 s19, s19, 0
	global_load_dword v182, v253, s[18:19]
	s_add_u32 s18, s18, 0x7000
	s_addc_u32 s19, s19, 0
	global_load_dword v183, v253, s[18:19]
	s_add_u32 s18, s18, 0x7000
	s_addc_u32 s19, s19, 0
	global_load_dword v184, v253, s[18:19]
	s_add_u32 s18, s18, 0x7000
	s_addc_u32 s19, s19, 0
	global_load_dword v185, v253, s[18:19]
	s_add_u32 s18, s18, 0x7000
	s_addc_u32 s19, s19, 0
	global_load_dword v186, v253, s[18:19]
	s_add_u32 s18, s18, 0x7000
	s_addc_u32 s19, s19, 0
	global_load_dword v187, v253, s[18:19]
	s_add_u32 s18, s18, 0x7000
	s_addc_u32 s19, s19, 0
	global_load_dword v188, v253, s[18:19]
	s_add_u32 s18, s18, 0x7000
	s_addc_u32 s19, s19, 0
	global_load_dword v189, v253, s[18:19]
	s_mov_b32 s100, 1

; __device__ __forceinline__ v6u pk32_fp6(const float (&x)[32]) {
;     v16f a, b;
; #pragma unroll
;     for (int i = 0; i < 16; ++i) { a[i] = __builtin_amdgcn_fmed3f(x[i], -7.5f, 7.5f); b[i] = __builtin_amdgcn_fmed3f(x[16 + i], -7.5f, 7.5f); }
;     return __builtin_amdgcn_cvt_scalef32_2xpk16_fp6_f32(a, b, 1.0f);
; }
; template <int MODE>
; __device__ __forceinline__ void tr_matrix6(const float* W, int nb, int K, int N, unsigned char* WT, int drows, int rot, int gw, int NGW, int lane, float wscale) {
;     ...
;         const int drow0 = (MODE == 0) ? n0 : ((n0 >> 7) * 256 + (n0 & 127) + (MODE == 2 ? 128 : 0));
;         unsigned char* dst = WT + (size_t)e * drows * K + (size_t)(drow0 + 4 * c) * K + k0 + 32 * q;
; #pragma unroll
;         for (int j = 0; j < 4; ++j) { float x[32];
; #pragma unroll
;             for (int i = 0; i < 32; ++i) x[i] = v[i][j] * wscale;
;             const v6u w = pk32_fp6(x);
;             *(u32x4*)(dst + (size_t)j * K) = (u32x4){w[0], w[1], w[2], w[3]}; *(u32x4*)(dst + (size_t)j * K + 16) = (u32x4){w[4], w[5], 0u, 0u}; }
.LBB0_1047:
	s_cmp_lg_u32 s100, 0
	s_cbranch_scc0 .Lf6_nostore
	s_and_b32 s18, s89, 3
	s_cmp_eq_u32 s18, 3
	s_cbranch_scc0 .Lf6_nostore
	s_mul_hi_u32 s18, s98, 0x2492493
	s_mul_i32 s19, s18, 0x70
	s_sub_u32 s19, s98, s19
	s_and_b32 s20, s18, 63
	s_lshr_b32 s18, s18, 6
	s_and_b32 s21, s18, 3
	s_add_u32 s21, s21, 4
	s_lshr_b32 s18, s18, 2
	s_lshr_b32 s101, s19, 1
	s_lshl_b32 s101, s101, 8
	s_and_b32 s19, s19, 1
	s_lshl_b32 s19, s19, 6
	s_add_u32 s19, s19, s101
	s_lshl_b32 s18, s18, 7
	s_add_u32 s19, s19, s18
	s_mul_i32 s21, s21, 0x3800
	s_add_u32 s19, s19, s21
	s_lshl_b32 s19, s19, 11
	s_lshl_b32 s20, s20, 5
	s_add_u32 s19, s19, s20
	s_add_u32 s19, s19, 0x8a00000
	s_add_u32 s20, s70, s19
	s_addc_u32 s21, s71, 0
	v_mbcnt_lo_u32_b32 v253, -1, 0
	v_mbcnt_hi_u32_b32 v253, -1, v253
	v_lshlrev_b32_e32 v253, 11, v253
	v_mov_b32_e32 v254, 0x40f00000
	s_mov_b32 s18, 0xc0f00000
	v_mov_b32_e32 v80, 0
	v_mov_b32_e32 v81, 0
	s_waitcnt vmcnt(0)
	v_mul_f32_e32 v158, 0x42b40000, v158
	v_mul_f32_e32 v159, 0x42b40000, v159
	v_mul_f32_e32 v160, 0x42b40000, v160
	v_mul_f32_e32 v161, 0x42b40000, v161
	v_mul_f32_e32 v162, 0x42b40000, v162
	v_mul_f32_e32 v163, 0x42b40000, v163
	v_mul_f32_e32 v164, 0x42b40000, v164
	v_mul_f32_e32 v165, 0x42b40000, v165
	v_mul_f32_e32 v166, 0x42b40000, v166
	v_mul_f32_e32 v167, 0x42b40000, v167
	v_mul_f32_e32 v168, 0x42b40000, v168
	v_mul_f32_e32 v169, 0x42b40000, v169
	v_mul_f32_e32 v170, 0x42b40000, v170
	v_mul_f32_e32 v171, 0x42b40000, v171
	v_mul_f32_e32 v172, 0x42b40000, v172
	v_mul_f32_e32 v173, 0x42b40000, v173
	v_mul_f32_e32 v174, 0x42b40000, v174
	v_mul_f32_e32 v175, 0x42b40000, v175
	v_mul_f32_e32 v176, 0x42b40000, v176
	v_mul_f32_e32 v177, 0x42b40000, v177
	v_mul_f32_e32 v178, 0x42b40000, v178
	v_mul_f32_e32 v179, 0x42b40000, v179
	v_mul_f32_e32 v180, 0x42b40000, v180
	v_mul_f32_e32 v181, 0x42b40000, v181
	v_mul_f32_e32 v182, 0x42b40000, v182
	v_mul_f32_e32 v183, 0x42b40000, v183
	v_mul_f32_e32 v184, 0x42b40000, v184
	v_mul_f32_e32 v185, 0x42b40000, v185
	v_mul_f32_e32 v186, 0x42b40000, v186
	v_mul_f32_e32 v187, 0x42b40000, v187
	v_mul_f32_e32 v188, 0x42b40000, v188
	v_mul_f32_e32 v189, 0x42b40000, v189
	v_med3_f32 v158, v158, s18, v254
	v_med3_f32 v159, v159, s18, v254
	v_med3_f32 v160, v160, s18, v254
	v_med3_f32 v161, v161, s18, v254
	v_med3_f32 v162, v162, s18, v254
	v_med3_f32 v163, v163, s18, v254
	v_med3_f32 v164, v164, s18, v254
	v_med3_f32 v165, v165, s18, v254
	v_med3_f32 v166, v166, s18, v254
	v_med3_f32 v167, v167, s18, v254
	v_med3_f32 v168, v168, s18, v254
	v_med3_f32 v169, v169, s18, v254
	v_med3_f32 v170, v170, s18, v254
	v_med3_f32 v171, v171, s18, v254
	v_med3_f32 v172, v172, s18, v254
	v_med3_f32 v173, v173, s18, v254
	v_med3_f32 v174, v174, s18, v254
	v_med3_f32 v175, v175, s18, v254
	v_med3_f32 v176, v176, s18, v254
	v_med3_f32 v177, v177, s18, v254
	v_med3_f32 v178, v178, s18, v254
	v_med3_f32 v179, v179, s18, v254
	v_med3_f32 v180, v180, s18, v254
	v_med3_f32 v181, v181, s18, v254
	v_med3_f32 v182, v182, s18, v254
	v_med3_f32 v183, v183, s18, v254
	v_med3_f32 v184, v184, s18, v254
	v_med3_f32 v185, v185, s18, v254
	v_med3_f32 v186, v186, s18, v254
	v_med3_f32 v187, v187, s18, v254
	v_med3_f32 v188, v188, s18, v254
	v_med3_f32 v189, v189, s18, v254
	v_cvt_scalef32_2xpk16_fp6_f32 v[74:79], v[158:173], v[174:189], 1.0
	s_nop 1
	global_store_dwordx4 v253, v[74:77], s[20:21]
	global_store_dwordx4 v253, v[78:81], s[20:21] offset:16
	s_add_i32 s98, s98, 1
	s_mov_b32 s100, 0

; template <int MODE>
; __device__ __forceinline__ void tr_matrix6(const float* W, int nb, int K, int N, unsigned char* WT, int drows, int rot, int gw, int NGW, int lane, float wscale) {
;     ...
;     for (; it < total; it += NGW) {
;         const int e = it / per, r = it - e * per, kb = r / nbn, nbk = r - kb * nbn, n0 = nbk * 32, k0 = kb * 256;
;         const float* src = W + (size_t)e * K * N + (size_t)(k0 + 32 * q) * N + n0 + 4 * c;
;         f32x4 v[32];
; #pragma unroll
;         for (int i = 0; i < 32; ++i) v[i] = *(const f32x4*)(src + (size_t)i * N);
.LBB0_1049:
	s_and_b32 s18, s89, 3
	s_cmp_eq_u32 s18, 2
	s_cbranch_scc0 .Lf6_noload_b
	s_cmp_lt_i32 s98, s99
	s_cbranch_scc0 .Lf6_noload_b
	s_cmp_lg_u32 s100, 0
	s_cbranch_scc1 .Lf6_noload_b
	s_mul_hi_u32 s18, s98, 0x2492493
	s_mul_i32 s19, s18, 0x70
	s_sub_u32 s19, s98, s19
	s_and_b32 s20, s18, 63
	s_lshr_b32 s18, s18, 6
	s_and_b32 s21, s18, 3
	s_add_u32 s21, s21, 4
	s_lshr_b32 s18, s18, 2
	s_lshl_b32 s21, s21, 11
	s_lshl_b32 s20, s20, 5
	s_add_u32 s21, s21, s20
	s_mul_i32 s21, s21, 0x7000
	s_lshl_b32 s19, s19, 8
	s_add_u32 s21, s21, s19
	s_lshl_b32 s20, s18, 1
	s_nop 3
	v_readlane_b32 s18, v252, s20
	s_add_u32 s20, s20, 1
	s_nop 3
	v_readlane_b32 s19, v252, s20
	s_nop 3
	s_add_u32 s18, s18, s21
	s_addc_u32 s19, s19, 0
	v_mbcnt_lo_u32_b32 v253, -1, 0
	v_mbcnt_hi_u32_b32 v253, -1, v253
	v_lshlrev_b32_e32 v253, 2, v253
	global_load_dword v158, v253, s[18:19]
	s_add_u32 s18, s18, 0x7000
	s_addc_u32 s19, s19, 0
	global_load_dword v159, v253, s[18:19]
	s_add_u32 s18, s18, 0x7000
	s_addc_u32 s19, s19, 0
	global_load_dword v160, v253, s[18:19]
	s_add_u32 s18, s18, 0x7000
	s_addc_u32 s19, s19, 0
	global_load_dword v161, v253, s[18:19]
	s_add_u32 s18, s18, 0x7000
	s_addc_u32 s19, s19, 0
	global_load_dword v162, v253, s[18:19]
	s_add_u32 s18, s18, 0x7000
	s_addc_u32 s19, s19, 0
	global_load_dword v163, v253, s[18:19]
	s_add_u32 s18, s18, 0x7000
	s_addc_u32 s19, s19, 0
	global_load_dword v164, v253, s[18:19]
	s_add_u32 s18, s18, 0x7000
	s_addc_u32 s19, s19, 0
	global_load_dword v165, v253, s[18:19]
	s_add_u32 s18, s18, 0x7000
	s_addc_u32 s19, s19, 0
	global_load_dword v166, v253, s[18:19]
	s_add_u32 s18, s18, 0x7000
	s_addc_u32 s19, s19, 0
	global_load_dword v167, v253, s[18:19]
	s_add_u32 s18, s18, 0x7000
	s_addc_u32 s19, s19, 0
	global_load_dword v168, v253, s[18:19]
	s_add_u32 s18, s18, 0x7000
	s_addc_u32 s19, s19, 0
	global_load_dword v169, v253, s[18:19]
	s_add_u32 s18, s18, 0x7000
	s_addc_u32 s19, s19, 0
	global_load_dword v170, v253, s[18:19]
	s_add_u32 s18, s18, 0x7000
	s_addc_u32 s19, s19, 0
	global_load_dword v171, v253, s[18:19]
	s_add_u32 s18, s18, 0x7000
	s_addc_u32 s19, s19, 0
	global_load_dword v172, v253, s[18:19]
	s_add_u32 s18, s18, 0x7000
	s_addc_u32 s19, s19, 0
	global_load_dword v173, v253, s[18:19]
	s_add_u32 s18, s18, 0x7000
	s_addc_u32 s19, s19, 0
	global_load_dword v174, v253, s[18:19]
	s_add_u32 s18, s18, 0x7000
	s_addc_u32 s19, s19, 0
	global_load_dword v175, v253, s[18:19]
	s_add_u32 s18, s18, 0x7000
	s_addc_u32 s19, s19, 0
	global_load_dword v176, v253, s[18:19]
	s_add_u32 s18, s18, 0x7000
	s_addc_u32 s19, s19, 0
	global_load_dword v177, v253, s[18:19]
	s_add_u32 s18, s18, 0x7000
	s_addc_u32 s19, s19, 0
	global_load_dword v178, v253, s[18:19]
	s_add_u32 s18, s18, 0x7000
	s_addc_u32 s19, s19, 0
	global_load_dword v179, v253, s[18:19]
	s_add_u32 s18, s18, 0x7000
	s_addc_u32 s19, s19, 0
	global_load_dword v180, v253, s[18:19]
	s_add_u32 s18, s18, 0x7000
	s_addc_u32 s19, s19, 0
	global_load_dword v181, v253, s[18:19]
	s_add_u32 s18, s18, 0x7000
	s_addc_u32 s19, s19, 0
	global_load_dword v182, v253, s[18:19]
	s_add_u32 s18, s18, 0x7000
	s_addc_u32 s19, s19, 0
	global_load_dword v183, v253, s[18:19]
	s_add_u32 s18, s18, 0x7000
	s_addc_u32 s19, s19, 0
	global_load_dword v184, v253, s[18:19]
	s_add_u32 s18, s18, 0x7000
	s_addc_u32 s19, s19, 0
	global_load_dword v185, v253, s[18:19]
	s_add_u32 s18, s18, 0x7000
	s_addc_u32 s19, s19, 0
	global_load_dword v186, v253, s[18:19]
	s_add_u32 s18, s18, 0x7000
	s_addc_u32 s19, s19, 0
	global_load_dword v187, v253, s[18:19]
	s_add_u32 s18, s18, 0x7000
	s_addc_u32 s19, s19, 0
	global_load_dword v188, v253, s[18:19]
	s_add_u32 s18, s18, 0x7000
	s_addc_u32 s19, s19, 0
	global_load_dword v189, v253, s[18:19]
	s_mov_b32 s100, 1
